# RCORE: drop redundant vmcnt(0) drain per chunk; G1 stage_scales loads pipelined
# speedup vs baseline: 1.0033x; 1.0033x over previous
; template <int VAR  >
; __device__ __forceinline__ void ret_core_mfma(const bf16* P, const bf16* VT, const float* decay_logit  , bf16* YF, bf16* YB, float* PT, LAS unsigned char* lds, const int tid, const int bid, const int G) {
;     ...
;             for (int js = 0; js < 4; ++js) { const v4u kw = vnx[js]; float kd[8];
;                 { const LAS f32x4* kp = (const LAS f32x4*)(lds + RC_TB + (32 * js + 8 * fqc) * 4); const f32x4 k0 = kp[0], k1 = kp[1];
;                   kd[0] = k0[0]; kd[1] = k0[1]; kd[2] = k0[2]; kd[3] = k0[3]; kd[4] = k1[0]; kd[5] = k1[1]; kd[6] = k1[2]; kd[7] = k1[3]; }
;                 v4u sw; sw.x = cvtpk(bflo(kw.x) * kd[0], bfhi(kw.x) * kd[1]); sw.y = cvtpk(bflo(kw.y) * kd[2], bfhi(kw.y) * kd[3]); sw.z = cvtpk(bflo(kw.z) * kd[4], bfhi(kw.z) * kd[5]); sw.w = cvtpk(bflo(kw.w) * kd[6], bfhi(kw.w) * kd[7]);
;                 Avs[js] = __builtin_bit_cast(bf16x8v, sw); }
; #pragma unroll
;             for (int n = 0; n < 16; ++n) acc4[n] = acc4[n] * cdec;
;             const int jj = 8 * fqc + (frc >> 2);
;             const unsigned trA = (unsigned)((jj >> 4) * 1024 + sl_swz((jj & 15) * 64 + 8 * (frc & 3))), trB = (unsigned)(((jj + 4) >> 4) * 1024 + sl_swz(((jj + 4) & 15) * 64 + 8 * (frc & 3)));
;             f32x4 accA[4][2], accY[4][2];
; #pragma unroll
;             for (int m = 0; m < 4; ++m)
; #pragma unroll
;                 for (int n = 0; n < 2; ++n) { accA[m][n] = (f32x4){0.f, 0.f, 0.f, 0.f}; accY[m][n] = (f32x4){0.f, 0.f, 0.f, 0.f}; }
; #pragma unroll
;             for (int ks = 0; ks < 8; ++ks) {
;                 if (ks < 4) { if (c == 0) RC_WAITV(6); else RC_WAITV(14); } else if (ks == 4) RC_WAITV(6); else if (ks == 5) RC_WAITV(5); else if (ks == 6) RC_WAITV(4); else RC_WAITV(3);
;                 RC_BAR();
;                 { const int s4 = RC_PREV(slot);
;                   if (ks + 4 < 12) RC_ISSUE(ks + 4, tok0, s4); else RC_ISSUE(ks + 4 - 12, tokn, s4); }
;                 bf16x8v At[4], Bk[2], Bs[2];
;                 const LAS unsigned char* sq = lds + RC_RG + slot * 16384;
; #pragma unroll
;                 for (int m = 0; m < 4; ++m) At[m] = *(const LAS bf16x8v*)(sq + aoff + m * 1024);
; #pragma unroll
;                 for (int n = 0; n < 2; ++n) { Bk[n] = *(const LAS bf16x8v*)(sq + 8192 + boff + n * 1024); Bs[n] = *(const LAS bf16x8v*)(lds + RC_ST + ks * 8192 + boff + n * 1024); }
; #pragma unroll
.LBB0_46:
	v_lshlrev_b32_e32 v116, 16, v88
	v_and_b32_e32 v117, 0xffff0000, v88
	v_lshlrev_b32_e32 v88, 16, v89
	v_and_b32_e32 v89, 0xffff0000, v89
	s_waitcnt lgkmcnt(0)
	v_pk_mul_f32 v[68:69], v[68:69], v[116:117]
	v_pk_mul_f32 v[70:71], v[70:71], v[88:89]
	v_cvt_pk_bf16_f32 v68, v68, v69
	v_cvt_pk_bf16_f32 v69, v70, v71
	v_lshlrev_b32_e32 v70, 16, v90
	v_and_b32_e32 v71, 0xffff0000, v90
	v_lshlrev_b32_e32 v88, 16, v91
	v_and_b32_e32 v89, 0xffff0000, v91
	v_pk_mul_f32 v[70:71], v[112:113], v[70:71]
	v_pk_mul_f32 v[88:89], v[114:115], v[88:89]
	v_cvt_pk_bf16_f32 v70, v70, v71
	v_cvt_pk_bf16_f32 v71, v88, v89
	v_lshlrev_b32_e32 v88, 16, v84
	v_and_b32_e32 v89, 0xffff0000, v84
	v_lshlrev_b32_e32 v84, 16, v85
	v_and_b32_e32 v85, 0xffff0000, v85
	v_pk_mul_f32 v[72:73], v[72:73], v[88:89]
	v_pk_mul_f32 v[74:75], v[74:75], v[84:85]
	v_cvt_pk_bf16_f32 v72, v72, v73
	v_cvt_pk_bf16_f32 v73, v74, v75
	v_lshlrev_b32_e32 v74, 16, v86
	v_and_b32_e32 v75, 0xffff0000, v86
	v_lshlrev_b32_e32 v84, 16, v87
	v_and_b32_e32 v85, 0xffff0000, v87
	v_pk_mul_f32 v[74:75], v[108:109], v[74:75]
	v_pk_mul_f32 v[84:85], v[110:111], v[84:85]
	v_cvt_pk_bf16_f32 v74, v74, v75
	v_cvt_pk_bf16_f32 v75, v84, v85
	v_lshlrev_b32_e32 v84, 16, v76
	v_and_b32_e32 v85, 0xffff0000, v76
	v_pk_mul_f32 v[84:85], v[104:105], v[84:85]
	s_add_i32 s38, s39, 1
	v_cvt_pk_bf16_f32 v76, v84, v85
	v_lshlrev_b32_e32 v84, 16, v77
	v_and_b32_e32 v85, 0xffff0000, v77
	v_pk_mul_f32 v[84:85], v[106:107], v[84:85]
	v_lshlrev_b32_e32 v226, 3, v215
	v_cvt_pk_bf16_f32 v77, v84, v85
	v_lshlrev_b32_e32 v84, 16, v78
	v_and_b32_e32 v85, 0xffff0000, v78
	v_pk_mul_f32 v[84:85], v[100:101], v[84:85]
	v_bfe_u32 v2, v230, 2, 2
	v_cvt_pk_bf16_f32 v78, v84, v85
	v_lshlrev_b32_e32 v84, 16, v79
	v_and_b32_e32 v85, 0xffff0000, v79
	v_pk_mul_f32 v[84:85], v[102:103], v[84:85]
	s_and_b64 s[6:7], s[4:5], exec
	v_cvt_pk_bf16_f32 v79, v84, v85
	v_lshlrev_b32_e32 v84, 16, v80
	v_and_b32_e32 v85, 0xffff0000, v80
	v_pk_mul_f32 v[84:85], v[96:97], v[84:85]
	v_or_b32_e32 v2, v226, v2
	v_cvt_pk_bf16_f32 v80, v84, v85
	v_lshlrev_b32_e32 v84, 16, v81
	v_and_b32_e32 v85, 0xffff0000, v81
	v_pk_mul_f32 v[84:85], v[98:99], v[84:85]
	v_and_b32_e32 v213, 3, v230
	v_cvt_pk_bf16_f32 v81, v84, v85
	v_lshlrev_b32_e32 v84, 16, v82
	v_and_b32_e32 v85, 0xffff0000, v82
	v_pk_mul_f32 v[84:85], v[92:93], v[84:85]
	v_lshlrev_b32_e32 v2, 6, v2
	v_cvt_pk_bf16_f32 v82, v84, v85
	v_lshlrev_b32_e32 v84, 16, v83
	v_and_b32_e32 v85, 0xffff0000, v83
	v_pk_mul_f32 v[84:85], v[94:95], v[84:85]
	s_movk_i32 s6, 0x2c0
	v_cvt_pk_bf16_f32 v83, v84, v85
	v_lshlrev_b32_e32 v84, 5, v230
	v_lshlrev_b32_e32 v85, 3, v213
	s_cselect_b32 s38, s33, s38
	v_and_b32_e32 v84, 0xfffffc00, v84
	v_and_or_b32 v2, v2, s6, v85
	v_lshlrev_b32_e32 v85, 5, v215
	v_and_or_b32 v84, v85, 32, v84
	s_movk_i32 s6, 0x120
	s_lshl_b32 s60, s38, 19
	v_bitop3_b32 v229, v84, s6, v2 bitop3:0x36
	v_lshl_add_u64 v[232:233], v[218:219], 0, s[60:61]
	s_mov_b64 s[6:7], 0x100
	s_lshl_b32 s40, s52, 14
	v_or_b32_e32 v234, v84, v2
	v_bitop3_b32 v227, v84, 32, v2 bitop3:0x36
	v_lshl_add_u64 v[84:85], v[232:233], 0, s[6:7]
	s_add_i32 s6, s40, 0xffffc000
	s_cmp_lg_u32 s52, 0
	s_cselect_b32 s6, s6, 0x10000
	s_add_i32 s6, s6, 0
	s_add_i32 s41, s6, s44
	s_barrier
	s_add_i32 m0, s41, 0x10000
	s_mov_b64 s[6:7], 0x900
	global_load_lds_dwordx4 v[84:85], off
	v_lshl_add_u64 v[84:85], v[232:233], 0, s[6:7]
	s_add_i32 m0, s41, 0x12000
	s_add_i32 s6, s40, 0
	global_load_lds_dwordx4 v[84:85], off
	s_add_i32 s7, s6, 0x10000
	v_add_u32_e32 v236, 0, v243
	v_add_u32_e32 v2, s7, v242
	ds_read_b128 v[144:147], v236 offset:1024
	ds_read_b128 v[136:139], v236
	ds_read_b128 v[96:99], v2
	ds_read_b128 v[112:115], v2 offset:1024
	ds_read_b128 v[128:131], v2 offset:2048
	ds_read_b128 v[148:151], v2 offset:3072
	v_add_u32_e32 v2, s7, v243
	ds_read_b128 v[132:135], v2 offset:8192
	ds_read_b128 v[140:143], v2 offset:9216
	v_mov_b32_e32 v217, v216
	v_pk_mul_f32 v[42:43], v[216:217], v[42:43]
	v_pk_mul_f32 v[40:41], v[224:225], v[40:41]
	v_pk_mul_f32 v[38:39], v[216:217], v[38:39]
	v_pk_mul_f32 v[36:37], v[224:225], v[36:37]
	v_or_b32_e32 v231, 0x100, v234
	s_add_i32 s6, s6, 0x12000
	s_waitcnt lgkmcnt(0)
	v_mfma_f32_16x16x32_bf16 v[84:87], v[132:135], v[96:99], 0
	v_add_u32_e32 v2, s6, v234
	v_add_u32_e32 v180, s6, v231
	v_add_u32_e32 v181, s6, v227
	v_mfma_f32_16x16x32_bf16 v[88:91], v[136:139], v[96:99], 0
	v_add_u32_e32 v182, s6, v229
	s_andn2_b64 vcc, exec, s[0:1]
	v_mfma_f32_16x16x32_bf16 v[92:95], v[140:143], v[96:99], 0
	v_mfma_f32_16x16x32_bf16 v[96:99], v[144:147], v[96:99], 0
	v_mfma_f32_16x16x32_bf16 v[100:103], v[132:135], v[112:115], 0
	v_mfma_f32_16x16x32_bf16 v[104:107], v[136:139], v[112:115], 0
	v_mfma_f32_16x16x32_bf16 v[108:111], v[140:143], v[112:115], 0
	v_mfma_f32_16x16x32_bf16 v[112:115], v[144:147], v[112:115], 0
	v_mfma_f32_16x16x32_bf16 v[116:119], v[132:135], v[128:131], 0
	v_mfma_f32_16x16x32_bf16 v[120:123], v[136:139], v[128:131], 0
	v_mfma_f32_16x16x32_bf16 v[124:127], v[140:143], v[128:131], 0
	v_mfma_f32_16x16x32_bf16 v[128:131], v[144:147], v[128:131], 0
	v_mfma_f32_16x16x32_bf16 v[132:135], v[132:135], v[148:151], 0
	v_mfma_f32_16x16x32_bf16 v[136:139], v[136:139], v[148:151], 0
	v_mfma_f32_16x16x32_bf16 v[140:143], v[140:143], v[148:151], 0
	v_mfma_f32_16x16x32_bf16 v[144:147], v[144:147], v[148:151], 0
	ds_read_b64_tr_b16 v[176:177], v2
	ds_read_b64_tr_b16 v[178:179], v180
	ds_read_b64_tr_b16 v[172:173], v181
	ds_read_b64_tr_b16 v[174:175], v182
	ds_read_b64_tr_b16 v[168:169], v2 offset:2048
	ds_read_b64_tr_b16 v[170:171], v180 offset:2048
	ds_read_b64_tr_b16 v[164:165], v181 offset:2048
	ds_read_b64_tr_b16 v[166:167], v182 offset:2048
	ds_read_b64_tr_b16 v[160:161], v2 offset:4096
	ds_read_b64_tr_b16 v[162:163], v180 offset:4096
	ds_read_b64_tr_b16 v[156:157], v181 offset:4096
	ds_read_b64_tr_b16 v[158:159], v182 offset:4096
	ds_read_b64_tr_b16 v[152:153], v2 offset:6144
	ds_read_b64_tr_b16 v[154:155], v180 offset:6144
	ds_read_b64_tr_b16 v[148:149], v181 offset:6144
	ds_read_b64_tr_b16 v[150:151], v182 offset:6144
	s_waitcnt lgkmcnt(0)
	v_cndmask_b32_e64 v2, 0, 1, s[0:1]
	v_cmp_ne_u32_e64 s[6:7], 1, v2
	v_mfma_f32_16x16x32_bf16 v[40:43], v[176:179], v[68:71], v[40:43]
	v_mfma_f32_16x16x32_bf16 v[36:39], v[172:175], v[68:71], v[36:39]
	v_mfma_f32_16x16x32_bf16 v[40:43], v[168:171], v[72:75], v[40:43]
	v_mfma_f32_16x16x32_bf16 v[36:39], v[164:167], v[72:75], v[36:39]
	v_mfma_f32_16x16x32_bf16 v[40:43], v[160:163], v[76:79], v[40:43]
	v_mfma_f32_16x16x32_bf16 v[36:39], v[156:159], v[76:79], v[36:39]
	v_mfma_f32_16x16x32_bf16 v[40:43], v[152:155], v[80:83], v[40:43]
	v_mfma_f32_16x16x32_bf16 v[36:39], v[148:151], v[80:83], v[36:39]
	s_cbranch_vccnz .LBB0_64
	s_waitcnt vmcnt(14)
	s_cbranch_execnz .LBB0_49

;     __host__ __device__ bool next(int i, Unit& u) const {
;         const long L = (long)i * G + c; if (L >= nwg) return false;
;         int wgid = (int)L; { const int q = nwg / NXCD, r = nwg % NXCD, xcd = wgid % NXCD, off = wgid / NXCD; wgid = (xcd < r ? xcd * (q + 1) : r * (q + 1) + (xcd - r) * q) + off; }
;         const int nig = WGM * nN, gid = wgid / nig, fm = gid * WGM, gsz = (nM - fm) < WGM ? (nM - fm) : WGM;
;         u.pm = fm + ((wgid % nig) % gsz); u.pn = (wgid % nig) / gsz; u.idx = i; return true;
; template <class Sched> __device__ __forceinline__ void stage_scales(PG8_LAS unsigned char* lds, const Sched& S, const float* rs, bool cols, int ldil, int tid) {
;     ...
;     if (tid < 256) { const int lper = 8 - ldil, c = tid, tm = ((c & ((1 << lper) - 1)) << ldil) + (c >> lper);
;         float eps = 1e-6f; asm volatile("" : "+s"(eps));
;         for (int i = 0; i < 16 && S.next(i, u); ++i) { const f32x4 a = *(const f32x4*)(rs + 4 * (size_t)(cols ? u.pn * BM + tm : u.pm * BM + tid));
;             tab[i * 256 + tid] = __builtin_amdgcn_rsqf(((a[0] + a[1]) + (a[2] + a[3])) * (1.0f / 1024.0f) + eps); } }
.LBB0_698:
	v_readlane_b32 s0, v255, 1
	v_readlane_b32 s1, v255, 2
	s_and_b64 vcc, exec, s[0:1]
	s_cbranch_vccz .LBB0_797
	v_readlane_b32 s0, v254, 59
	s_cmp_gt_i32 s0, 0
	s_mov_b64 s[0:1], -1
	s_cbranch_scc0 .LBB0_735
	v_mbcnt_lo_u32_b32 v16, -1, 0
	v_mbcnt_hi_u32_b32 v16, -1, v16
	s_movk_i32 s0, 0x100
	v_add_u32_e32 v1, s30, v16
	v_cmp_gt_i32_e32 vcc, s0, v1
	s_and_saveexec_b64 s[0:1], vcc
	s_cbranch_execz .LBB0_718
	s_mov_b32 s4, 0x358637bd
	s_cmpk_gt_i32 s90, 0xaff
	s_cbranch_scc1 .LBB0_718
	s_ashr_i32 s3, s90, 31
	s_lshr_b32 s2, s3, 29
	s_add_i32 s2, s90, s2
	s_ashr_i32 s6, s2, 3
	s_and_b32 s2, s2, -8
	s_ashr_i32 s5, s88, 31
	s_sub_i32 s2, s90, s2
	s_cmp_lt_i32 s2, 0
	s_movk_i32 s7, 0x161
	s_cselect_b32 s7, s7, 0x160
	s_mul_i32 s2, s2, s7
	s_add_i32 s2, s2, s6
	s_mul_hi_i32 s6, s2, 0x2e8ba2e9
	s_lshr_b32 s7, s6, 31
	s_ashr_i32 s6, s6, 5
	s_add_i32 s6, s6, s7
	s_lshl_b32 s7, s6, 3
	s_sub_i32 s8, 0x80, s7
	s_min_i32 s8, s8, 8
	s_abs_i32 s8, s8
	v_cvt_f32_u32_e32 v0, s8
	s_sub_i32 s9, 0, s8
	s_mulk_i32 s6, 0xb0
	s_sub_i32 s2, s2, s6
	v_rcp_iflag_f32_e32 v0, v0
	s_ashr_i32 s6, s2, 31
	s_abs_i32 s2, s2
	v_mov_b32_e32 v2, s4
	v_mul_f32_e32 v0, 0x4f7ffffe, v0
	v_cvt_u32_f32_e32 v0, v0
	s_nop 0
	v_readfirstlane_b32 s10, v0
	s_mul_i32 s9, s9, s10
	s_mul_hi_u32 s9, s10, s9
	s_add_i32 s10, s10, s9
	s_mul_hi_u32 s9, s2, s10
	s_mul_i32 s9, s9, s8
	s_sub_i32 s2, s2, s9
	s_sub_i32 s9, s2, s8
	s_cmp_ge_u32 s2, s8
	s_cselect_b32 s2, s9, s2
	s_sub_i32 s9, s2, s8
	s_cmp_ge_u32 s2, s8
	s_cselect_b32 s2, s9, s2
	s_xor_b32 s2, s2, s6
	s_sub_i32 s2, s2, s6
	s_add_i32 s7, s7, s2
	v_lshl_add_u32 v4, s7, 8, v1
	v_readlane_b32 s6, v254, 63
	s_waitcnt lgkmcnt(0)
	v_ashrrev_i32_e32 v5, 31, v4
	v_readlane_b32 s7, v255, 0
	s_add_u32 s2, s88, s90
	s_addc_u32 s3, s5, s3
	v_lshl_add_u64 v[4:5], v[4:5], 4, s[6:7]
	global_load_dwordx4 v[64:67], v[4:5], off
	v_lshl_add_u32 v0, v1, 2, 0
	v_add_u32_e32 v0, 0x20000, v0
	v_mov_b64_e32 v[4:5], 0xaff
	v_cmp_gt_i64_e32 vcc, s[2:3], v[4:5]
	s_cbranch_vccnz .LBB0_718
	s_ashr_i32 s6, s2, 31
	s_lshr_b32 s6, s6, 29
	s_add_i32 s6, s2, s6
	s_ashr_i32 s7, s6, 3
	s_and_b32 s6, s6, -8
	s_sub_i32 s6, s2, s6
	s_cmp_lt_i32 s6, 0
	s_movk_i32 s8, 0x161
	s_cselect_b32 s8, s8, 0x160
	s_mul_i32 s6, s6, s8
	s_add_i32 s6, s6, s7
	s_mul_hi_i32 s7, s6, 0x2e8ba2e9
	s_lshr_b32 s8, s7, 31
	s_ashr_i32 s7, s7, 5
	s_add_i32 s7, s7, s8
	s_lshl_b32 s8, s7, 3
	s_sub_i32 s9, 0x80, s8
	s_min_i32 s9, s9, 8
	s_abs_i32 s9, s9
	v_cvt_f32_u32_e32 v2, s9
	s_sub_i32 s10, 0, s9
	s_mulk_i32 s7, 0xb0
	s_sub_i32 s6, s6, s7
	v_rcp_iflag_f32_e32 v2, v2
	s_ashr_i32 s7, s6, 31
	s_abs_i32 s6, s6
	v_mul_f32_e32 v2, 0x4f7ffffe, v2
	v_cvt_u32_f32_e32 v2, v2
	s_nop 0
	v_readfirstlane_b32 s11, v2
	s_mul_i32 s10, s10, s11
	s_mul_hi_u32 s10, s11, s10
	s_add_i32 s11, s11, s10
	s_mul_hi_u32 s10, s6, s11
	s_mul_i32 s10, s10, s9
	s_sub_i32 s6, s6, s10
	s_sub_i32 s10, s6, s9
	s_cmp_ge_u32 s6, s9
	s_cselect_b32 s6, s10, s6
	s_sub_i32 s10, s6, s9
	s_cmp_ge_u32 s6, s9
	s_cselect_b32 s6, s10, s6
	s_xor_b32 s6, s6, s7
	s_sub_i32 s6, s6, s7
	s_add_i32 s8, s8, s6
	v_lshl_add_u32 v4, s8, 8, v1
	v_readlane_b32 s6, v254, 63
	v_ashrrev_i32_e32 v5, 31, v4
	v_readlane_b32 s7, v255, 0
	v_mov_b32_e32 v2, s4
	s_add_u32 s2, s2, s88
	v_lshl_add_u64 v[4:5], v[4:5], 4, s[6:7]
	global_load_dwordx4 v[68:71], v[4:5], off
	s_addc_u32 s3, s3, s5
	v_mov_b64_e32 v[4:5], 0xaff
	v_cmp_gt_i64_e32 vcc, s[2:3], v[4:5]
	s_cbranch_vccnz .LBB0_718
	s_ashr_i32 s6, s2, 31
	s_lshr_b32 s6, s6, 29
	s_add_i32 s6, s2, s6
	s_ashr_i32 s7, s6, 3
	s_and_b32 s6, s6, -8
	s_sub_i32 s6, s2, s6
	s_cmp_lt_i32 s6, 0
	s_movk_i32 s8, 0x161
	s_cselect_b32 s8, s8, 0x160
	s_mul_i32 s6, s6, s8
	s_add_i32 s6, s6, s7
	s_mul_hi_i32 s7, s6, 0x2e8ba2e9
	s_lshr_b32 s8, s7, 31
	s_ashr_i32 s7, s7, 5
	s_add_i32 s7, s7, s8
	s_lshl_b32 s8, s7, 3
	s_sub_i32 s9, 0x80, s8
	s_min_i32 s9, s9, 8
	s_abs_i32 s9, s9
	v_cvt_f32_u32_e32 v2, s9
	s_sub_i32 s10, 0, s9
	s_mulk_i32 s7, 0xb0
	s_sub_i32 s6, s6, s7
	v_rcp_iflag_f32_e32 v2, v2
	s_ashr_i32 s7, s6, 31
	s_abs_i32 s6, s6
	v_mul_f32_e32 v2, 0x4f7ffffe, v2
	v_cvt_u32_f32_e32 v2, v2
	s_nop 0
	v_readfirstlane_b32 s11, v2
	s_mul_i32 s10, s10, s11
	s_mul_hi_u32 s10, s11, s10
	s_add_i32 s11, s11, s10
	s_mul_hi_u32 s10, s6, s11
	s_mul_i32 s10, s10, s9
	s_sub_i32 s6, s6, s10
	s_sub_i32 s10, s6, s9
	s_cmp_ge_u32 s6, s9
	s_cselect_b32 s6, s10, s6
	s_sub_i32 s10, s6, s9
	s_cmp_ge_u32 s6, s9
	s_cselect_b32 s6, s10, s6
	s_xor_b32 s6, s6, s7
	s_sub_i32 s6, s6, s7
	s_add_i32 s8, s8, s6
	v_lshl_add_u32 v4, s8, 8, v1
	v_readlane_b32 s6, v254, 63
	v_ashrrev_i32_e32 v5, 31, v4
	v_readlane_b32 s7, v255, 0
	v_mov_b32_e32 v2, s4
	s_add_u32 s2, s2, s88
	v_lshl_add_u64 v[4:5], v[4:5], 4, s[6:7]
	global_load_dwordx4 v[72:75], v[4:5], off
	s_addc_u32 s3, s3, s5
	v_mov_b64_e32 v[4:5], 0xaff
	v_cmp_gt_i64_e32 vcc, s[2:3], v[4:5]
	s_cbranch_vccnz .LBB0_718
	s_ashr_i32 s6, s2, 31
	s_lshr_b32 s6, s6, 29
	s_add_i32 s6, s2, s6
	s_ashr_i32 s7, s6, 3
	s_and_b32 s6, s6, -8
	s_sub_i32 s6, s2, s6
	s_cmp_lt_i32 s6, 0
	s_movk_i32 s8, 0x161
	s_cselect_b32 s8, s8, 0x160
	s_mul_i32 s6, s6, s8
	s_add_i32 s6, s6, s7
	s_mul_hi_i32 s7, s6, 0x2e8ba2e9
	s_lshr_b32 s8, s7, 31
	s_ashr_i32 s7, s7, 5
	s_add_i32 s7, s7, s8
	s_lshl_b32 s8, s7, 3
	s_sub_i32 s9, 0x80, s8
	s_min_i32 s9, s9, 8
	s_abs_i32 s9, s9
	v_cvt_f32_u32_e32 v2, s9
	s_sub_i32 s10, 0, s9
	s_mulk_i32 s7, 0xb0
	s_sub_i32 s6, s6, s7
	v_rcp_iflag_f32_e32 v2, v2
	s_ashr_i32 s7, s6, 31
	s_abs_i32 s6, s6
	v_mul_f32_e32 v2, 0x4f7ffffe, v2
	v_cvt_u32_f32_e32 v2, v2
	s_nop 0
	v_readfirstlane_b32 s11, v2
	s_mul_i32 s10, s10, s11
	s_mul_hi_u32 s10, s11, s10
	s_add_i32 s11, s11, s10
	s_mul_hi_u32 s10, s6, s11
	s_mul_i32 s10, s10, s9
	s_sub_i32 s6, s6, s10
	s_sub_i32 s10, s6, s9
	s_cmp_ge_u32 s6, s9
	s_cselect_b32 s6, s10, s6
	s_sub_i32 s10, s6, s9
	s_cmp_ge_u32 s6, s9
	s_cselect_b32 s6, s10, s6
	s_xor_b32 s6, s6, s7
	s_sub_i32 s6, s6, s7
	s_add_i32 s8, s8, s6
	v_lshl_add_u32 v4, s8, 8, v1
	v_readlane_b32 s6, v254, 63
	v_ashrrev_i32_e32 v5, 31, v4
	v_readlane_b32 s7, v255, 0
	v_mov_b32_e32 v2, s4
	s_add_u32 s2, s2, s88
	v_lshl_add_u64 v[4:5], v[4:5], 4, s[6:7]
	global_load_dwordx4 v[76:79], v[4:5], off
	s_addc_u32 s3, s3, s5
	v_mov_b64_e32 v[4:5], 0xaff
	v_cmp_gt_i64_e32 vcc, s[2:3], v[4:5]
	s_cbranch_vccnz .LBB0_718
;     __host__ __device__ bool next(int i, Unit& u) const {
;         const long L = (long)i * G + c; if (L >= nwg) return false;
;         int wgid = (int)L; { const int q = nwg / NXCD, r = nwg % NXCD, xcd = wgid % NXCD, off = wgid / NXCD; wgid = (xcd < r ? xcd * (q + 1) : r * (q + 1) + (xcd - r) * q) + off; }
;         const int nig = WGM * nN, gid = wgid / nig, fm = gid * WGM, gsz = (nM - fm) < WGM ? (nM - fm) : WGM;
;         u.pm = fm + ((wgid % nig) % gsz); u.pn = (wgid % nig) / gsz; u.idx = i; return true;
; template <class Sched> __device__ __forceinline__ void stage_scales(PG8_LAS unsigned char* lds, const Sched& S, const float* rs, bool cols, int ldil, int tid) {
;     ...
;     if (tid < 256) { const int lper = 8 - ldil, c = tid, tm = ((c & ((1 << lper) - 1)) << ldil) + (c >> lper);
;         float eps = 1e-6f; asm volatile("" : "+s"(eps));
;         for (int i = 0; i < 16 && S.next(i, u); ++i) { const f32x4 a = *(const f32x4*)(rs + 4 * (size_t)(cols ? u.pn * BM + tm : u.pm * BM + tid));
;             tab[i * 256 + tid] = __builtin_amdgcn_rsqf(((a[0] + a[1]) + (a[2] + a[3])) * (1.0f / 1024.0f) + eps); } }
	s_ashr_i32 s6, s2, 31
	s_lshr_b32 s6, s6, 29
	s_add_i32 s6, s2, s6
	s_ashr_i32 s7, s6, 3
	s_and_b32 s6, s6, -8
	s_sub_i32 s6, s2, s6
	s_cmp_lt_i32 s6, 0
	s_movk_i32 s8, 0x161
	s_cselect_b32 s8, s8, 0x160
	s_mul_i32 s6, s6, s8
	s_add_i32 s6, s6, s7
	s_mul_hi_i32 s7, s6, 0x2e8ba2e9
	s_lshr_b32 s8, s7, 31
	s_ashr_i32 s7, s7, 5
	s_add_i32 s7, s7, s8
	s_lshl_b32 s8, s7, 3
	s_sub_i32 s9, 0x80, s8
	s_min_i32 s9, s9, 8
	s_abs_i32 s9, s9
	v_cvt_f32_u32_e32 v2, s9
	s_sub_i32 s10, 0, s9
	s_mulk_i32 s7, 0xb0
	s_sub_i32 s6, s6, s7
	v_rcp_iflag_f32_e32 v2, v2
	s_ashr_i32 s7, s6, 31
	s_abs_i32 s6, s6
	v_mul_f32_e32 v2, 0x4f7ffffe, v2
	v_cvt_u32_f32_e32 v2, v2
	s_nop 0
	v_readfirstlane_b32 s11, v2
	s_mul_i32 s10, s10, s11
	s_mul_hi_u32 s10, s11, s10
	s_add_i32 s11, s11, s10
	s_mul_hi_u32 s10, s6, s11
	s_mul_i32 s10, s10, s9
	s_sub_i32 s6, s6, s10
	s_sub_i32 s10, s6, s9
	s_cmp_ge_u32 s6, s9
	s_cselect_b32 s6, s10, s6
	s_sub_i32 s10, s6, s9
	s_cmp_ge_u32 s6, s9
	s_cselect_b32 s6, s10, s6
	s_xor_b32 s6, s6, s7
	s_sub_i32 s6, s6, s7
	s_add_i32 s8, s8, s6
	v_lshl_add_u32 v4, s8, 8, v1
	v_readlane_b32 s6, v254, 63
	v_ashrrev_i32_e32 v5, 31, v4
	v_readlane_b32 s7, v255, 0
	v_mov_b32_e32 v2, s4
	s_add_u32 s2, s2, s88
	v_lshl_add_u64 v[4:5], v[4:5], 4, s[6:7]
	global_load_dwordx4 v[80:83], v[4:5], off
	s_addc_u32 s3, s3, s5
	v_mov_b64_e32 v[4:5], 0xaff
	v_cmp_gt_i64_e32 vcc, s[2:3], v[4:5]
	s_cbranch_vccnz .LBB0_718
	s_ashr_i32 s6, s2, 31
	s_lshr_b32 s6, s6, 29
	s_add_i32 s6, s2, s6
	s_ashr_i32 s7, s6, 3
	s_and_b32 s6, s6, -8
	s_sub_i32 s6, s2, s6
	s_cmp_lt_i32 s6, 0
	s_movk_i32 s8, 0x161
	s_cselect_b32 s8, s8, 0x160
	s_mul_i32 s6, s6, s8
	s_add_i32 s6, s6, s7
	s_mul_hi_i32 s7, s6, 0x2e8ba2e9
	s_lshr_b32 s8, s7, 31
	s_ashr_i32 s7, s7, 5
	s_add_i32 s7, s7, s8
	s_lshl_b32 s8, s7, 3
	s_sub_i32 s9, 0x80, s8
	s_min_i32 s9, s9, 8
	s_abs_i32 s9, s9
	v_cvt_f32_u32_e32 v2, s9
	s_sub_i32 s10, 0, s9
	s_mulk_i32 s7, 0xb0
	s_sub_i32 s6, s6, s7
	v_rcp_iflag_f32_e32 v2, v2
	s_ashr_i32 s7, s6, 31
	s_abs_i32 s6, s6
	v_mul_f32_e32 v2, 0x4f7ffffe, v2
	v_cvt_u32_f32_e32 v2, v2
	s_nop 0
	v_readfirstlane_b32 s11, v2
	s_mul_i32 s10, s10, s11
	s_mul_hi_u32 s10, s11, s10
	s_add_i32 s11, s11, s10
	s_mul_hi_u32 s10, s6, s11
	s_mul_i32 s10, s10, s9
	s_sub_i32 s6, s6, s10
	s_sub_i32 s10, s6, s9
	s_cmp_ge_u32 s6, s9
	s_cselect_b32 s6, s10, s6
	s_sub_i32 s10, s6, s9
	s_cmp_ge_u32 s6, s9
	s_cselect_b32 s6, s10, s6
	s_xor_b32 s6, s6, s7
	s_sub_i32 s6, s6, s7
	s_add_i32 s8, s8, s6
	v_lshl_add_u32 v4, s8, 8, v1
	v_readlane_b32 s6, v254, 63
	v_ashrrev_i32_e32 v5, 31, v4
	v_readlane_b32 s7, v255, 0
	v_mov_b32_e32 v2, s4
	s_add_u32 s2, s2, s88
	v_lshl_add_u64 v[4:5], v[4:5], 4, s[6:7]
	global_load_dwordx4 v[84:87], v[4:5], off
	s_addc_u32 s3, s3, s5
	v_mov_b64_e32 v[4:5], 0xaff
	v_cmp_gt_i64_e32 vcc, s[2:3], v[4:5]
	s_cbranch_vccnz .LBB0_718
	s_ashr_i32 s6, s2, 31
	s_lshr_b32 s6, s6, 29
	s_add_i32 s6, s2, s6
	s_ashr_i32 s7, s6, 3
	s_and_b32 s6, s6, -8
	s_sub_i32 s6, s2, s6
	s_cmp_lt_i32 s6, 0
	s_movk_i32 s8, 0x161
	s_cselect_b32 s8, s8, 0x160
	s_mul_i32 s6, s6, s8
	s_add_i32 s6, s6, s7
	s_mul_hi_i32 s7, s6, 0x2e8ba2e9
	s_lshr_b32 s8, s7, 31
	s_ashr_i32 s7, s7, 5
	s_add_i32 s7, s7, s8
	s_lshl_b32 s8, s7, 3
	s_sub_i32 s9, 0x80, s8
	s_min_i32 s9, s9, 8
	s_abs_i32 s9, s9
	v_cvt_f32_u32_e32 v2, s9
	s_sub_i32 s10, 0, s9
	s_mulk_i32 s7, 0xb0
	s_sub_i32 s6, s6, s7
	v_rcp_iflag_f32_e32 v2, v2
	s_ashr_i32 s7, s6, 31
	s_abs_i32 s6, s6
	v_mul_f32_e32 v2, 0x4f7ffffe, v2
	v_cvt_u32_f32_e32 v2, v2
	s_nop 0
	v_readfirstlane_b32 s11, v2
	s_mul_i32 s10, s10, s11
	s_mul_hi_u32 s10, s11, s10
	s_add_i32 s11, s11, s10
	s_mul_hi_u32 s10, s6, s11
	s_mul_i32 s10, s10, s9
	s_sub_i32 s6, s6, s10
	s_sub_i32 s10, s6, s9
	s_cmp_ge_u32 s6, s9
	s_cselect_b32 s6, s10, s6
	s_sub_i32 s10, s6, s9
	s_cmp_ge_u32 s6, s9
	s_cselect_b32 s6, s10, s6
	s_xor_b32 s6, s6, s7
	s_sub_i32 s6, s6, s7
	s_add_i32 s8, s8, s6
	v_lshl_add_u32 v4, s8, 8, v1
	v_readlane_b32 s6, v254, 63
	v_ashrrev_i32_e32 v5, 31, v4
	v_readlane_b32 s7, v255, 0
	v_mov_b32_e32 v2, s4
	s_add_u32 s2, s2, s88
	v_lshl_add_u64 v[4:5], v[4:5], 4, s[6:7]
	global_load_dwordx4 v[88:91], v[4:5], off
	s_addc_u32 s3, s3, s5
	v_mov_b64_e32 v[4:5], 0xaff
	v_cmp_gt_i64_e32 vcc, s[2:3], v[4:5]
	s_cbranch_vccnz .LBB0_718
	s_ashr_i32 s6, s2, 31
	s_lshr_b32 s6, s6, 29
	s_add_i32 s6, s2, s6
	s_ashr_i32 s7, s6, 3
	s_and_b32 s6, s6, -8
	s_sub_i32 s6, s2, s6
	s_cmp_lt_i32 s6, 0
	s_movk_i32 s8, 0x161
	s_cselect_b32 s8, s8, 0x160
	s_mul_i32 s6, s6, s8
	s_add_i32 s6, s6, s7
	s_mul_hi_i32 s7, s6, 0x2e8ba2e9
	s_lshr_b32 s8, s7, 31
	s_ashr_i32 s7, s7, 5
	s_add_i32 s7, s7, s8
	s_lshl_b32 s8, s7, 3
	s_sub_i32 s9, 0x80, s8
	s_min_i32 s9, s9, 8
	s_abs_i32 s9, s9
	v_cvt_f32_u32_e32 v2, s9
	s_sub_i32 s10, 0, s9
	s_mulk_i32 s7, 0xb0
	s_sub_i32 s6, s6, s7
	v_rcp_iflag_f32_e32 v2, v2
	s_ashr_i32 s7, s6, 31
	s_abs_i32 s6, s6
	v_mul_f32_e32 v2, 0x4f7ffffe, v2
	v_cvt_u32_f32_e32 v2, v2
	s_nop 0
	v_readfirstlane_b32 s11, v2
	s_mul_i32 s10, s10, s11
	s_mul_hi_u32 s10, s11, s10
	s_add_i32 s11, s11, s10
	s_mul_hi_u32 s10, s6, s11
	s_mul_i32 s10, s10, s9
	s_sub_i32 s6, s6, s10
	s_sub_i32 s10, s6, s9
	s_cmp_ge_u32 s6, s9
	s_cselect_b32 s6, s10, s6
	s_sub_i32 s10, s6, s9
	s_cmp_ge_u32 s6, s9
	s_cselect_b32 s6, s10, s6
	s_xor_b32 s6, s6, s7
	s_sub_i32 s6, s6, s7
	s_add_i32 s8, s8, s6
	v_lshl_add_u32 v4, s8, 8, v1
	v_readlane_b32 s6, v254, 63
	v_ashrrev_i32_e32 v5, 31, v4
	v_readlane_b32 s7, v255, 0
	v_mov_b32_e32 v2, s4
	s_add_u32 s2, s2, s88
	v_lshl_add_u64 v[4:5], v[4:5], 4, s[6:7]
	global_load_dwordx4 v[92:95], v[4:5], off
	s_addc_u32 s3, s3, s5
	v_mov_b64_e32 v[4:5], 0xaff
	v_cmp_gt_i64_e32 vcc, s[2:3], v[4:5]
	s_cbranch_vccnz .LBB0_718
;     __host__ __device__ bool next(int i, Unit& u) const {
;         const long L = (long)i * G + c; if (L >= nwg) return false;
;         int wgid = (int)L; { const int q = nwg / NXCD, r = nwg % NXCD, xcd = wgid % NXCD, off = wgid / NXCD; wgid = (xcd < r ? xcd * (q + 1) : r * (q + 1) + (xcd - r) * q) + off; }
;         const int nig = WGM * nN, gid = wgid / nig, fm = gid * WGM, gsz = (nM - fm) < WGM ? (nM - fm) : WGM;
;         u.pm = fm + ((wgid % nig) % gsz); u.pn = (wgid % nig) / gsz; u.idx = i; return true;
; template <class Sched> __device__ __forceinline__ void stage_scales(PG8_LAS unsigned char* lds, const Sched& S, const float* rs, bool cols, int ldil, int tid) {
;     ...
;     if (tid < 256) { const int lper = 8 - ldil, c = tid, tm = ((c & ((1 << lper) - 1)) << ldil) + (c >> lper);
;         float eps = 1e-6f; asm volatile("" : "+s"(eps));
;         for (int i = 0; i < 16 && S.next(i, u); ++i) { const f32x4 a = *(const f32x4*)(rs + 4 * (size_t)(cols ? u.pn * BM + tm : u.pm * BM + tid));
;             tab[i * 256 + tid] = __builtin_amdgcn_rsqf(((a[0] + a[1]) + (a[2] + a[3])) * (1.0f / 1024.0f) + eps); } }
	s_ashr_i32 s6, s2, 31
	s_lshr_b32 s6, s6, 29
	s_add_i32 s6, s2, s6
	s_ashr_i32 s7, s6, 3
	s_and_b32 s6, s6, -8
	s_sub_i32 s6, s2, s6
	s_cmp_lt_i32 s6, 0
	s_movk_i32 s8, 0x161
	s_cselect_b32 s8, s8, 0x160
	s_mul_i32 s6, s6, s8
	s_add_i32 s6, s6, s7
	s_mul_hi_i32 s7, s6, 0x2e8ba2e9
	s_lshr_b32 s8, s7, 31
	s_ashr_i32 s7, s7, 5
	s_add_i32 s7, s7, s8
	s_lshl_b32 s8, s7, 3
	s_sub_i32 s9, 0x80, s8
	s_min_i32 s9, s9, 8
	s_abs_i32 s9, s9
	v_cvt_f32_u32_e32 v2, s9
	s_sub_i32 s10, 0, s9
	s_mulk_i32 s7, 0xb0
	s_sub_i32 s6, s6, s7
	v_rcp_iflag_f32_e32 v2, v2
	s_ashr_i32 s7, s6, 31
	s_abs_i32 s6, s6
	v_mul_f32_e32 v2, 0x4f7ffffe, v2
	v_cvt_u32_f32_e32 v2, v2
	s_nop 0
	v_readfirstlane_b32 s11, v2
	s_mul_i32 s10, s10, s11
	s_mul_hi_u32 s10, s11, s10
	s_add_i32 s11, s11, s10
	s_mul_hi_u32 s10, s6, s11
	s_mul_i32 s10, s10, s9
	s_sub_i32 s6, s6, s10
	s_sub_i32 s10, s6, s9
	s_cmp_ge_u32 s6, s9
	s_cselect_b32 s6, s10, s6
	s_sub_i32 s10, s6, s9
	s_cmp_ge_u32 s6, s9
	s_cselect_b32 s6, s10, s6
	s_xor_b32 s6, s6, s7
	s_sub_i32 s6, s6, s7
	s_add_i32 s8, s8, s6
	v_lshl_add_u32 v4, s8, 8, v1
	v_readlane_b32 s6, v254, 63
	v_ashrrev_i32_e32 v5, 31, v4
	v_readlane_b32 s7, v255, 0
	v_mov_b32_e32 v2, s4
	s_add_u32 s2, s2, s88
	v_lshl_add_u64 v[4:5], v[4:5], 4, s[6:7]
	global_load_dwordx4 v[96:99], v[4:5], off
	s_addc_u32 s3, s3, s5
	v_mov_b64_e32 v[4:5], 0xaff
	v_cmp_gt_i64_e32 vcc, s[2:3], v[4:5]
	s_cbranch_vccnz .LBB0_718
	s_ashr_i32 s6, s2, 31
	s_lshr_b32 s6, s6, 29
	s_add_i32 s6, s2, s6
	s_ashr_i32 s7, s6, 3
	s_and_b32 s6, s6, -8
	s_sub_i32 s6, s2, s6
	s_cmp_lt_i32 s6, 0
	s_movk_i32 s8, 0x161
	s_cselect_b32 s8, s8, 0x160
	s_mul_i32 s6, s6, s8
	s_add_i32 s6, s6, s7
	s_mul_hi_i32 s7, s6, 0x2e8ba2e9
	s_lshr_b32 s8, s7, 31
	s_ashr_i32 s7, s7, 5
	s_add_i32 s7, s7, s8
	s_lshl_b32 s8, s7, 3
	s_sub_i32 s9, 0x80, s8
	s_min_i32 s9, s9, 8
	s_abs_i32 s9, s9
	v_cvt_f32_u32_e32 v2, s9
	s_sub_i32 s10, 0, s9
	s_mulk_i32 s7, 0xb0
	s_sub_i32 s6, s6, s7
	v_rcp_iflag_f32_e32 v2, v2
	s_ashr_i32 s7, s6, 31
	s_abs_i32 s6, s6
	v_mul_f32_e32 v2, 0x4f7ffffe, v2
	v_cvt_u32_f32_e32 v2, v2
	s_nop 0
	v_readfirstlane_b32 s11, v2
	s_mul_i32 s10, s10, s11
	s_mul_hi_u32 s10, s11, s10
	s_add_i32 s11, s11, s10
	s_mul_hi_u32 s10, s6, s11
	s_mul_i32 s10, s10, s9
	s_sub_i32 s6, s6, s10
	s_sub_i32 s10, s6, s9
	s_cmp_ge_u32 s6, s9
	s_cselect_b32 s6, s10, s6
	s_sub_i32 s10, s6, s9
	s_cmp_ge_u32 s6, s9
	s_cselect_b32 s6, s10, s6
	s_xor_b32 s6, s6, s7
	s_sub_i32 s6, s6, s7
	s_add_i32 s8, s8, s6
	v_lshl_add_u32 v4, s8, 8, v1
	v_readlane_b32 s6, v254, 63
	v_ashrrev_i32_e32 v5, 31, v4
	v_readlane_b32 s7, v255, 0
	v_mov_b32_e32 v2, s4
	s_add_u32 s2, s2, s88
	v_lshl_add_u64 v[4:5], v[4:5], 4, s[6:7]
	global_load_dwordx4 v[100:103], v[4:5], off
	s_addc_u32 s3, s3, s5
	v_mov_b64_e32 v[4:5], 0xaff
	v_cmp_gt_i64_e32 vcc, s[2:3], v[4:5]
	s_cbranch_vccnz .LBB0_718
	s_ashr_i32 s6, s2, 31
	s_lshr_b32 s6, s6, 29
	s_add_i32 s6, s2, s6
	s_ashr_i32 s7, s6, 3
	s_and_b32 s6, s6, -8
	s_sub_i32 s6, s2, s6
	s_cmp_lt_i32 s6, 0
	s_movk_i32 s8, 0x161
	s_cselect_b32 s8, s8, 0x160
	s_mul_i32 s6, s6, s8
	s_add_i32 s6, s6, s7
	s_mul_hi_i32 s7, s6, 0x2e8ba2e9
	s_lshr_b32 s8, s7, 31
	s_ashr_i32 s7, s7, 5
	s_add_i32 s7, s7, s8
	s_lshl_b32 s8, s7, 3
	s_sub_i32 s9, 0x80, s8
	s_min_i32 s9, s9, 8
	s_abs_i32 s9, s9
	v_cvt_f32_u32_e32 v2, s9
	s_sub_i32 s10, 0, s9
	s_mulk_i32 s7, 0xb0
	s_sub_i32 s6, s6, s7
	v_rcp_iflag_f32_e32 v2, v2
	s_ashr_i32 s7, s6, 31
	s_abs_i32 s6, s6
	v_mul_f32_e32 v2, 0x4f7ffffe, v2
	v_cvt_u32_f32_e32 v2, v2
	s_nop 0
	v_readfirstlane_b32 s11, v2
	s_mul_i32 s10, s10, s11
	s_mul_hi_u32 s10, s11, s10
	s_add_i32 s11, s11, s10
	s_mul_hi_u32 s10, s6, s11
	s_mul_i32 s10, s10, s9
	s_sub_i32 s6, s6, s10
	s_sub_i32 s10, s6, s9
	s_cmp_ge_u32 s6, s9
	s_cselect_b32 s6, s10, s6
	s_sub_i32 s10, s6, s9
	s_cmp_ge_u32 s6, s9
	s_cselect_b32 s6, s10, s6
	s_xor_b32 s6, s6, s7
	s_sub_i32 s6, s6, s7
	s_add_i32 s8, s8, s6
	v_lshl_add_u32 v4, s8, 8, v1
	v_readlane_b32 s6, v254, 63
	v_ashrrev_i32_e32 v5, 31, v4
	v_readlane_b32 s7, v255, 0
	v_mov_b32_e32 v2, s4
	s_add_u32 s2, s2, s88
	v_lshl_add_u64 v[4:5], v[4:5], 4, s[6:7]
	global_load_dwordx4 v[104:107], v[4:5], off
	s_addc_u32 s3, s3, s5
	v_mov_b64_e32 v[4:5], 0xaff
	v_cmp_gt_i64_e32 vcc, s[2:3], v[4:5]
	s_cbranch_vccnz .LBB0_718
	s_ashr_i32 s6, s2, 31
	s_lshr_b32 s6, s6, 29
	s_add_i32 s6, s2, s6
	s_ashr_i32 s7, s6, 3
	s_and_b32 s6, s6, -8
	s_sub_i32 s6, s2, s6
	s_cmp_lt_i32 s6, 0
	s_movk_i32 s8, 0x161
	s_cselect_b32 s8, s8, 0x160
	s_mul_i32 s6, s6, s8
	s_add_i32 s6, s6, s7
	s_mul_hi_i32 s7, s6, 0x2e8ba2e9
	s_lshr_b32 s8, s7, 31
	s_ashr_i32 s7, s7, 5
	s_add_i32 s7, s7, s8
	s_lshl_b32 s8, s7, 3
	s_sub_i32 s9, 0x80, s8
	s_min_i32 s9, s9, 8
	s_abs_i32 s9, s9
	v_cvt_f32_u32_e32 v2, s9
	s_sub_i32 s10, 0, s9
	s_mulk_i32 s7, 0xb0
	s_sub_i32 s6, s6, s7
	v_rcp_iflag_f32_e32 v2, v2
	s_ashr_i32 s7, s6, 31
	s_abs_i32 s6, s6
	v_mul_f32_e32 v2, 0x4f7ffffe, v2
	v_cvt_u32_f32_e32 v2, v2
	s_nop 0
	v_readfirstlane_b32 s11, v2
	s_mul_i32 s10, s10, s11
	s_mul_hi_u32 s10, s11, s10
	s_add_i32 s11, s11, s10
	s_mul_hi_u32 s10, s6, s11
	s_mul_i32 s10, s10, s9
	s_sub_i32 s6, s6, s10
	s_sub_i32 s10, s6, s9
	s_cmp_ge_u32 s6, s9
	s_cselect_b32 s6, s10, s6
	s_sub_i32 s10, s6, s9
	s_cmp_ge_u32 s6, s9
	s_cselect_b32 s6, s10, s6
	s_xor_b32 s6, s6, s7
	s_sub_i32 s6, s6, s7
	s_add_i32 s8, s8, s6
	v_lshl_add_u32 v4, s8, 8, v1
	v_readlane_b32 s6, v254, 63
	v_ashrrev_i32_e32 v5, 31, v4
	v_readlane_b32 s7, v255, 0
	v_mov_b32_e32 v2, s4
	s_add_u32 s2, s2, s88
	v_lshl_add_u64 v[4:5], v[4:5], 4, s[6:7]
	global_load_dwordx4 v[108:111], v[4:5], off
	s_addc_u32 s3, s3, s5
	v_mov_b64_e32 v[4:5], 0xaff
	v_cmp_gt_i64_e32 vcc, s[2:3], v[4:5]
	s_cbranch_vccnz .LBB0_718
;     __host__ __device__ bool next(int i, Unit& u) const {
;         const long L = (long)i * G + c; if (L >= nwg) return false;
;         int wgid = (int)L; { const int q = nwg / NXCD, r = nwg % NXCD, xcd = wgid % NXCD, off = wgid / NXCD; wgid = (xcd < r ? xcd * (q + 1) : r * (q + 1) + (xcd - r) * q) + off; }
;         const int nig = WGM * nN, gid = wgid / nig, fm = gid * WGM, gsz = (nM - fm) < WGM ? (nM - fm) : WGM;
;         u.pm = fm + ((wgid % nig) % gsz); u.pn = (wgid % nig) / gsz; u.idx = i; return true;
; template <class Sched> __device__ __forceinline__ void stage_scales(PG8_LAS unsigned char* lds, const Sched& S, const float* rs, bool cols, int ldil, int tid) {
;     ...
;     if (tid < 256) { const int lper = 8 - ldil, c = tid, tm = ((c & ((1 << lper) - 1)) << ldil) + (c >> lper);
;         float eps = 1e-6f; asm volatile("" : "+s"(eps));
;         for (int i = 0; i < 16 && S.next(i, u); ++i) { const f32x4 a = *(const f32x4*)(rs + 4 * (size_t)(cols ? u.pn * BM + tm : u.pm * BM + tid));
;             tab[i * 256 + tid] = __builtin_amdgcn_rsqf(((a[0] + a[1]) + (a[2] + a[3])) * (1.0f / 1024.0f) + eps); } }
	s_ashr_i32 s6, s2, 31
	s_lshr_b32 s6, s6, 29
	s_add_i32 s6, s2, s6
	s_ashr_i32 s7, s6, 3
	s_and_b32 s6, s6, -8
	s_sub_i32 s6, s2, s6
	s_cmp_lt_i32 s6, 0
	s_movk_i32 s8, 0x161
	s_cselect_b32 s8, s8, 0x160
	s_mul_i32 s6, s6, s8
	s_add_i32 s6, s6, s7
	s_mul_hi_i32 s7, s6, 0x2e8ba2e9
	s_lshr_b32 s8, s7, 31
	s_ashr_i32 s7, s7, 5
	s_add_i32 s7, s7, s8
	s_lshl_b32 s8, s7, 3
	s_sub_i32 s9, 0x80, s8
	s_min_i32 s9, s9, 8
	s_abs_i32 s9, s9
	v_cvt_f32_u32_e32 v2, s9
	s_sub_i32 s10, 0, s9
	s_mulk_i32 s7, 0xb0
	s_sub_i32 s6, s6, s7
	v_rcp_iflag_f32_e32 v2, v2
	s_ashr_i32 s7, s6, 31
	s_abs_i32 s6, s6
	v_mul_f32_e32 v2, 0x4f7ffffe, v2
	v_cvt_u32_f32_e32 v2, v2
	s_nop 0
	v_readfirstlane_b32 s11, v2
	s_mul_i32 s10, s10, s11
	s_mul_hi_u32 s10, s11, s10
	s_add_i32 s11, s11, s10
	s_mul_hi_u32 s10, s6, s11
	s_mul_i32 s10, s10, s9
	s_sub_i32 s6, s6, s10
	s_sub_i32 s10, s6, s9
	s_cmp_ge_u32 s6, s9
	s_cselect_b32 s6, s10, s6
	s_sub_i32 s10, s6, s9
	s_cmp_ge_u32 s6, s9
	s_cselect_b32 s6, s10, s6
	s_xor_b32 s6, s6, s7
	s_sub_i32 s6, s6, s7
	s_add_i32 s8, s8, s6
	v_lshl_add_u32 v4, s8, 8, v1
	v_readlane_b32 s6, v254, 63
	v_ashrrev_i32_e32 v5, 31, v4
	v_readlane_b32 s7, v255, 0
	v_mov_b32_e32 v2, s4
	s_add_u32 s2, s2, s88
	v_lshl_add_u64 v[4:5], v[4:5], 4, s[6:7]
	global_load_dwordx4 v[112:115], v[4:5], off
	s_addc_u32 s3, s3, s5
	v_mov_b64_e32 v[4:5], 0xaff
	v_cmp_gt_i64_e32 vcc, s[2:3], v[4:5]
	s_cbranch_vccnz .LBB0_718
	s_ashr_i32 s6, s2, 31
	s_lshr_b32 s6, s6, 29
	s_add_i32 s6, s2, s6
	s_ashr_i32 s7, s6, 3
	s_and_b32 s6, s6, -8
	s_sub_i32 s6, s2, s6
	s_cmp_lt_i32 s6, 0
	s_movk_i32 s8, 0x161
	s_cselect_b32 s8, s8, 0x160
	s_mul_i32 s6, s6, s8
	s_add_i32 s6, s6, s7
	s_mul_hi_i32 s7, s6, 0x2e8ba2e9
	s_lshr_b32 s8, s7, 31
	s_ashr_i32 s7, s7, 5
	s_add_i32 s7, s7, s8
	s_lshl_b32 s8, s7, 3
	s_sub_i32 s9, 0x80, s8
	s_min_i32 s9, s9, 8
	s_abs_i32 s9, s9
	v_cvt_f32_u32_e32 v2, s9
	s_sub_i32 s10, 0, s9
	s_mulk_i32 s7, 0xb0
	s_sub_i32 s6, s6, s7
	v_rcp_iflag_f32_e32 v2, v2
	s_ashr_i32 s7, s6, 31
	s_abs_i32 s6, s6
	v_mul_f32_e32 v2, 0x4f7ffffe, v2
	v_cvt_u32_f32_e32 v2, v2
	s_nop 0
	v_readfirstlane_b32 s11, v2
	s_mul_i32 s10, s10, s11
	s_mul_hi_u32 s10, s11, s10
	s_add_i32 s11, s11, s10
	s_mul_hi_u32 s10, s6, s11
	s_mul_i32 s10, s10, s9
	s_sub_i32 s6, s6, s10
	s_sub_i32 s10, s6, s9
	s_cmp_ge_u32 s6, s9
	s_cselect_b32 s6, s10, s6
	s_sub_i32 s10, s6, s9
	s_cmp_ge_u32 s6, s9
	s_cselect_b32 s6, s10, s6
	s_xor_b32 s6, s6, s7
	s_sub_i32 s6, s6, s7
	s_add_i32 s8, s8, s6
	v_lshl_add_u32 v4, s8, 8, v1
	v_readlane_b32 s6, v254, 63
	v_ashrrev_i32_e32 v5, 31, v4
	v_readlane_b32 s7, v255, 0
	v_mov_b32_e32 v2, s4
	s_add_u32 s2, s2, s88
	v_lshl_add_u64 v[4:5], v[4:5], 4, s[6:7]
	global_load_dwordx4 v[116:119], v[4:5], off
	s_addc_u32 s3, s3, s5
	v_mov_b64_e32 v[4:5], 0xaff
	v_cmp_gt_i64_e32 vcc, s[2:3], v[4:5]
	s_cbranch_vccnz .LBB0_718
	s_ashr_i32 s6, s2, 31
	s_lshr_b32 s6, s6, 29
	s_add_i32 s6, s2, s6
	s_ashr_i32 s7, s6, 3
	s_and_b32 s6, s6, -8
	s_sub_i32 s6, s2, s6
	s_cmp_lt_i32 s6, 0
	s_movk_i32 s8, 0x161
	s_cselect_b32 s8, s8, 0x160
	s_mul_i32 s6, s6, s8
	s_add_i32 s6, s6, s7
	s_mul_hi_i32 s7, s6, 0x2e8ba2e9
	s_lshr_b32 s8, s7, 31
	s_ashr_i32 s7, s7, 5
	s_add_i32 s7, s7, s8
	s_lshl_b32 s8, s7, 3
	s_sub_i32 s9, 0x80, s8
	s_min_i32 s9, s9, 8
	s_abs_i32 s9, s9
	v_cvt_f32_u32_e32 v2, s9
	s_sub_i32 s10, 0, s9
	s_mulk_i32 s7, 0xb0
	s_sub_i32 s6, s6, s7
	v_rcp_iflag_f32_e32 v2, v2
	s_ashr_i32 s7, s6, 31
	s_abs_i32 s6, s6
	v_mul_f32_e32 v2, 0x4f7ffffe, v2
	v_cvt_u32_f32_e32 v2, v2
	s_nop 0
	v_readfirstlane_b32 s11, v2
	s_mul_i32 s10, s10, s11
	s_mul_hi_u32 s10, s11, s10
	s_add_i32 s11, s11, s10
	s_mul_hi_u32 s10, s6, s11
	s_mul_i32 s10, s10, s9
	s_sub_i32 s6, s6, s10
	s_sub_i32 s10, s6, s9
	s_cmp_ge_u32 s6, s9
	s_cselect_b32 s6, s10, s6
	s_sub_i32 s10, s6, s9
	s_cmp_ge_u32 s6, s9
	s_cselect_b32 s6, s10, s6
	s_xor_b32 s6, s6, s7
	s_sub_i32 s6, s6, s7
	s_add_i32 s8, s8, s6
	v_lshl_add_u32 v4, s8, 8, v1
	v_readlane_b32 s6, v254, 63
	v_ashrrev_i32_e32 v5, 31, v4
	v_readlane_b32 s7, v255, 0
	v_mov_b32_e32 v2, s4
	s_add_u32 s2, s2, s88
	v_lshl_add_u64 v[4:5], v[4:5], 4, s[6:7]
	global_load_dwordx4 v[120:123], v[4:5], off
	s_addc_u32 s3, s3, s5
	v_mov_b64_e32 v[4:5], 0xaff
	v_cmp_gt_i64_e32 vcc, s[2:3], v[4:5]
	s_cbranch_vccnz .LBB0_718
	s_ashr_i32 s3, s2, 31
	s_lshr_b32 s3, s3, 29
	s_add_i32 s3, s2, s3
	s_ashr_i32 s5, s3, 3
	s_and_b32 s3, s3, -8
	s_sub_i32 s2, s2, s3
	s_cmp_lt_i32 s2, 0
	s_movk_i32 s3, 0x161
	s_cselect_b32 s3, s3, 0x160
	s_mul_i32 s2, s2, s3
	s_add_i32 s2, s2, s5
	s_mul_hi_i32 s3, s2, 0x2e8ba2e9
	s_lshr_b32 s5, s3, 31
	s_ashr_i32 s3, s3, 5
	s_add_i32 s3, s3, s5
	s_lshl_b32 s5, s3, 3
	s_sub_i32 s6, 0x80, s5
	s_min_i32 s6, s6, 8
	s_abs_i32 s6, s6
	v_cvt_f32_u32_e32 v2, s6
	s_sub_i32 s7, 0, s6
	s_mulk_i32 s3, 0xb0
	s_sub_i32 s2, s2, s3
	v_rcp_iflag_f32_e32 v2, v2
	s_ashr_i32 s3, s2, 31
	s_abs_i32 s2, s2
	v_mul_f32_e32 v2, 0x4f7ffffe, v2
	v_cvt_u32_f32_e32 v2, v2
	s_nop 0
	v_readfirstlane_b32 s8, v2
	s_mul_i32 s7, s7, s8
	s_mul_hi_u32 s7, s8, s7
	s_add_i32 s8, s8, s7
	s_mul_hi_u32 s7, s2, s8
	s_mul_i32 s7, s7, s6
	s_sub_i32 s2, s2, s7
	s_sub_i32 s7, s2, s6
	s_cmp_ge_u32 s2, s6
	s_cselect_b32 s2, s7, s2
	s_sub_i32 s7, s2, s6
	s_cmp_ge_u32 s2, s6
	s_cselect_b32 s2, s7, s2
	s_xor_b32 s2, s2, s3
	s_sub_i32 s2, s2, s3
	s_add_i32 s5, s5, s2
	v_lshl_add_u32 v4, s5, 8, v1
	v_readlane_b32 s2, v254, 63
	v_ashrrev_i32_e32 v5, 31, v4
	v_readlane_b32 s3, v255, 0
	s_nop 1
	v_lshl_add_u64 v[4:5], v[4:5], 4, s[2:3]
	global_load_dwordx4 v[124:127], v[4:5], off
; template <class Sched> __device__ __forceinline__ void stage_scales(PG8_LAS unsigned char* lds, const Sched& S, const float* rs, bool cols, int ldil, int tid) {
;     ...
;         for (int i = 0; i < 16 && S.next(i, u); ++i) { const f32x4 a = *(const f32x4*)(rs + 4 * (size_t)(cols ? u.pn * BM + tm : u.pm * BM + tid));
;             tab[i * 256 + tid] = __builtin_amdgcn_rsqf(((a[0] + a[1]) + (a[2] + a[3])) * (1.0f / 1024.0f) + eps); } }
;     __syncthreads();
.LBB0_718:
	s_waitcnt vmcnt(0)
	v_mov_b32_e32 v2, s4
	v_add_f32_e32 v8, v64, v65
	v_add_f32_e32 v9, v66, v67
	v_add_f32_e32 v8, v8, v9
	v_fmamk_f32 v8, v8, 0x3a800000, v2
	v_rsq_f32_e32 v8, v8
	s_nop 1
	ds_write_b32 v0, v8
	v_add_f32_e32 v8, v68, v69
	v_add_f32_e32 v9, v70, v71
	v_add_f32_e32 v8, v8, v9
	v_fmamk_f32 v8, v8, 0x3a800000, v2
	v_rsq_f32_e32 v8, v8
	s_nop 1
	ds_write_b32 v0, v8 offset:1024
	v_add_f32_e32 v8, v72, v73
	v_add_f32_e32 v9, v74, v75
	v_add_f32_e32 v8, v8, v9
	v_fmamk_f32 v8, v8, 0x3a800000, v2
	v_rsq_f32_e32 v8, v8
	s_nop 1
	ds_write_b32 v0, v8 offset:2048
	v_add_f32_e32 v8, v76, v77
	v_add_f32_e32 v9, v78, v79
	v_add_f32_e32 v8, v8, v9
	v_fmamk_f32 v8, v8, 0x3a800000, v2
	v_rsq_f32_e32 v8, v8
	s_nop 1
	ds_write_b32 v0, v8 offset:3072
	v_add_f32_e32 v8, v80, v81
	v_add_f32_e32 v9, v82, v83
	v_add_f32_e32 v8, v8, v9
	v_fmamk_f32 v8, v8, 0x3a800000, v2
	v_rsq_f32_e32 v8, v8
	s_nop 1
	ds_write_b32 v0, v8 offset:4096
	v_add_f32_e32 v8, v84, v85
	v_add_f32_e32 v9, v86, v87
	v_add_f32_e32 v8, v8, v9
	v_fmamk_f32 v8, v8, 0x3a800000, v2
	v_rsq_f32_e32 v8, v8
	s_nop 1
	ds_write_b32 v0, v8 offset:5120
	v_add_f32_e32 v8, v88, v89
	v_add_f32_e32 v9, v90, v91
	v_add_f32_e32 v8, v8, v9
	v_fmamk_f32 v8, v8, 0x3a800000, v2
	v_rsq_f32_e32 v8, v8
	s_nop 1
	ds_write_b32 v0, v8 offset:6144
	v_add_f32_e32 v8, v92, v93
	v_add_f32_e32 v9, v94, v95
	v_add_f32_e32 v8, v8, v9
	v_fmamk_f32 v8, v8, 0x3a800000, v2
	v_rsq_f32_e32 v8, v8
	s_nop 1
	ds_write_b32 v0, v8 offset:7168
	v_add_f32_e32 v8, v96, v97
	v_add_f32_e32 v9, v98, v99
	v_add_f32_e32 v8, v8, v9
	v_fmamk_f32 v8, v8, 0x3a800000, v2
	v_rsq_f32_e32 v8, v8
	s_nop 1
	ds_write_b32 v0, v8 offset:8192
	v_add_f32_e32 v8, v100, v101
	v_add_f32_e32 v9, v102, v103
	v_add_f32_e32 v8, v8, v9
	v_fmamk_f32 v8, v8, 0x3a800000, v2
	v_rsq_f32_e32 v8, v8
	s_nop 1
	ds_write_b32 v0, v8 offset:9216
	v_add_f32_e32 v8, v104, v105
	v_add_f32_e32 v9, v106, v107
	v_add_f32_e32 v8, v8, v9
	v_fmamk_f32 v8, v8, 0x3a800000, v2
	v_rsq_f32_e32 v8, v8
	s_nop 1
	ds_write_b32 v0, v8 offset:10240
	v_add_f32_e32 v8, v108, v109
	v_add_f32_e32 v9, v110, v111
	v_add_f32_e32 v8, v8, v9
	v_fmamk_f32 v8, v8, 0x3a800000, v2
	v_rsq_f32_e32 v8, v8
	s_nop 1
	ds_write_b32 v0, v8 offset:11264
	v_add_f32_e32 v8, v112, v113
	v_add_f32_e32 v9, v114, v115
	v_add_f32_e32 v8, v8, v9
	v_fmamk_f32 v8, v8, 0x3a800000, v2
	v_rsq_f32_e32 v8, v8
	s_nop 1
	ds_write_b32 v0, v8 offset:12288
	v_add_f32_e32 v8, v116, v117
	v_add_f32_e32 v9, v118, v119
	v_add_f32_e32 v8, v8, v9
	v_fmamk_f32 v8, v8, 0x3a800000, v2
	v_rsq_f32_e32 v8, v8
	s_nop 1
	ds_write_b32 v0, v8 offset:13312
	v_add_f32_e32 v8, v120, v121
	v_add_f32_e32 v9, v122, v123
	v_add_f32_e32 v8, v8, v9
	v_fmamk_f32 v8, v8, 0x3a800000, v2
	v_rsq_f32_e32 v8, v8
	s_nop 1
	ds_write_b32 v0, v8 offset:14336
	v_add_f32_e32 v8, v124, v125
	v_add_f32_e32 v9, v126, v127
	v_add_f32_e32 v8, v8, v9
	v_fmamk_f32 v8, v8, 0x3a800000, v2
	v_rsq_f32_e32 v8, v8
	s_nop 1
	ds_write_b32 v0, v8 offset:15360
	s_or_b64 exec, exec, s[0:1]
	s_cmpk_gt_i32 s90, 0xaff
	v_readfirstlane_b32 s3, v1
	s_waitcnt vmcnt(0) lgkmcnt(0)
	s_barrier
	s_cbranch_scc1 .LBB0_734
; #define PG8_STAGE(bufoff, gbase, voff) do { _Pragma("unroll") for (int _i = 0; _i < 2; ++_i) \
;         __builtin_amdgcn_global_load_lds((const unsigned*)((const char*)(gbase) + (voff)[_i]), (PG8_LAS unsigned*)(lds + (bufoff) + ldsw + _i * 8192), 16, 0, 0); } while (0)
; #define PG8_BAR __builtin_amdgcn_s_barrier()
; template <class Epi, class Sched, bool ALIGN_EPI = false, bool SP2 = false>
; __device__ __forceinline__ void gemm_phase(PG8_LAS unsigned char* lds, const Gemm g, const Sched& S, const Epi& E, const int tid) {
;     ...
;     for (int i = 0; i < 2; ++i) { int R, C; stage_rc(tid * 16 + i * 8192, R, C); const int Rb = Epi::PERM ? ((R & ~31) + perm32(R & 31)) : R;
;         voffA[i] = (unsigned)(R * K + C) * 2u; { const int ld = g.ldil, lper = 8 - ld, pm1 = (1 << lper) - 1; const int c0 = Rb, c1 = 128 + Rb; voffB[i] = (unsigned)((((c0 & pm1) << ld) + (c0 >> lper)) * K + C) * 2u; voffB1[i] = (unsigned)((((c1 & pm1) << ld) + (c1 >> lper)) * K + C) * 2u; } }
;     const size_t kstep = (size_t)(BK * 2);
;     const size_t hstep = (size_t)HALF * K * 2;
;     const size_t tstep = 2 * hstep;
;     const unsigned ldsw = (unsigned)wid * 1024u;
;     const int aoff = lds_byte(wr * 64 + fr, fq * 8), boff = lds_byte(wc * 32 + fr, fq * 8);
;     ...
;     Unit cur, nxt; int ui = 0;
;     if (!S.next(0, cur)) return;
;     f32x4 acc[2][2][4][2];
; #pragma unroll
;     for (int a = 0; a < 2; ++a)
; #pragma unroll
;         for (int b = 0; b < 2; ++b)
; #pragma unroll
;             for (int m = 0; m < 4; ++m)
; #pragma unroll
;                 for (int n = 0; n < 2; ++n) acc[a][b][m][n] = (f32x4){0.f, 0.f, 0.f, 0.f};
;     bf16x8 At[4][2], B0[2][2], B1[2][2];
;     const char* cA = (const char*)g.A + (size_t)cur.pm * tstep; const char* cB = (const char*)g.Bt + (size_t)cur.pn * tstep;
;     S.a_ready(cur);
;     if constexpr (SP2) {
;         PG8_STAGE(PG8_SB(0, 0), cB, voffB); PG8_STAGE(PG8_SB(0, 1), cB, voffB1); PG8_STAGE(PG8_SA(0, 0), cA, voffA); PG8_STAGE(PG8_SA(0, 1), cA + hstep, voffA);
;         if (wr == 1) PG8_BAR;
	v_lshlrev_b32_e32 v2, 4, v1
	v_add_u32_e32 v0, 0x2000, v2
	v_ashrrev_i32_e32 v4, 31, v0
	v_lshrrev_b32_e32 v4, 22, v4
	v_add_u32_e32 v4, v0, v4
	v_ashrrev_i32_e32 v17, 10, v4
	v_mul_i32_i24_e32 v4, 0x400, v17
	v_sub_u32_e32 v0, v0, v4
	v_lshrrev_b32_e32 v4, 4, v0
	v_bitop3_b32 v0, v4, v0, 32 bitop3:0x6c
	v_ashrrev_i32_e32 v4, 31, v0
	v_lshrrev_b32_e32 v4, 26, v4
	v_add_u32_e32 v4, v0, v4
	v_lshlrev_b32_e32 v5, 3, v17
	v_ashrrev_i32_e32 v18, 6, v4
	v_and_b32_e32 v5, -16, v5
	v_add_u32_e32 v5, v18, v5
	v_lshrrev_b32_e32 v8, 2, v5
	v_and_b32_e32 v6, 0xffffffe0, v5
	v_and_b32_e32 v7, 3, v18
	v_and_b32_e32 v8, 4, v8
	v_or3_b32 v6, v6, v7, v8
	v_lshlrev_b32_e32 v7, 1, v5
	s_ashr_i32 s6, s3, 6
	v_and_b32_e32 v7, 24, v7
	s_ashr_i32 s7, s3, 8
	s_lshl_b32 s33, s6, 10
	v_or_b32_e32 v8, v6, v7
	s_add_u32 s38, s96, 0x1a00000
	v_add_u32_e32 v8, 0x80, v8
	v_and_b32_e32 v4, 0xc0, v4
	s_addc_u32 s39, s97, 0
	v_lshrrev_b32_e32 v9, 8, v8
	v_sub_u32_e32 v0, v0, v4
	s_add_u32 s40, s96, 0x200000
	v_add_u32_sdwa v8, v8, v9 dst_sel:DWORD dst_unused:UNUSED_PAD src0_sel:BYTE_0 src1_sel:DWORD
	v_lshlrev_b32_e32 v9, 5, v17
	v_ashrrev_i16_sdwa v0, v235, sext(v0) dst_sel:DWORD dst_unused:UNUSED_PAD src0_sel:DWORD src1_sel:BYTE_0
	s_addc_u32 s41, s97, 0
	v_and_b32_e32 v9, 32, v9
	v_bfe_i32 v19, v0, 0, 16
	v_bitop3_b32 v6, v6, s70, v7 bitop3:0xc8
	v_lshrrev_b32_e32 v7, 8, v5
	s_ashr_i32 s42, s90, 31
	v_add_lshl_u32 v4, v9, v19, 1
	v_add_u32_e32 v6, v6, v7
	s_lshr_b32 s0, s42, 29
	v_lshl_add_u32 v0, v8, 11, v4
	v_lshl_add_u32 v132, v6, 11, v4
	v_lshl_add_u32 v134, v5, 11, v4
	v_bfe_i32 v4, v1, 27, 1
	s_add_i32 s0, s90, s0
	v_lshrrev_b32_e32 v4, 22, v4
	s_ashr_i32 s1, s0, 3
	s_and_b32 s0, s0, -8
	v_add_u32_e32 v4, v2, v4
	s_sub_i32 s0, s90, s0
	v_and_b32_e32 v4, 0xfffffc00, v4
	s_cmp_lt_i32 s0, 0
	s_movk_i32 s2, 0x161
	v_sub_u32_e32 v2, v2, v4
	s_cselect_b32 s2, s2, 0x160
	v_lshrrev_b32_e32 v4, 4, v2
	v_ashrrev_i32_e32 v5, 31, v1
	s_mul_i32 s0, s0, s2
	v_bitop3_b32 v2, v4, v2, 32 bitop3:0x6c
	v_lshrrev_b32_e32 v5, 26, v5
	s_add_i32 s0, s0, s1
	v_ashrrev_i32_e32 v4, 31, v2
	v_add_u32_e32 v1, v1, v5
	s_mul_hi_i32 s1, s0, 0x2e8ba2e9
	v_lshrrev_b32_e32 v4, 26, v4
	v_ashrrev_i32_e32 v21, 6, v1
	s_lshr_b32 s2, s1, 31
	s_ashr_i32 s1, s1, 5
	v_add_u32_e32 v4, v2, v4
	v_lshlrev_b32_e32 v1, 3, v21
	s_add_i32 s1, s1, s2
	v_ashrrev_i32_e32 v20, 6, v4
	v_and_b32_e32 v1, -16, v1
	s_lshl_b32 s4, s1, 3
	s_mulk_i32 s1, 0xb0
	v_add_u32_e32 v1, v20, v1
	s_sub_i32 s0, s0, s1
	v_lshrrev_b32_e32 v7, 2, v1
	s_bfe_u32 s1, s0, 0x3001c
	v_and_b32_e32 v5, 0xffffffe0, v1
	v_and_b32_e32 v6, 3, v20
	v_and_b32_e32 v7, 4, v7
	s_add_i32 s1, s0, s1
	v_or3_b32 v5, v5, v6, v7
	v_lshlrev_b32_e32 v6, 1, v1
	s_sext_i32_i16 s2, s1
	s_and_b32 s1, s1, 0xfff8
	v_and_b32_e32 v6, 24, v6
	s_sub_i32 s0, s0, s1
	v_or_b32_e32 v7, v5, v6
	s_sext_i32_i16 s0, s0
	v_add_u32_e32 v7, 0x80, v7
	v_and_b32_e32 v4, 0xc0, v4
	s_lshr_b32 s2, s2, 3
	s_add_i32 s44, s4, s0
	v_lshrrev_b32_e32 v8, 8, v7
	v_sub_u32_e32 v2, v2, v4
	s_ashr_i32 s45, s44, 31
	s_bfe_i64 s[4:5], s[2:3], 0x100000
	v_add_u32_sdwa v7, v7, v8 dst_sel:DWORD dst_unused:UNUSED_PAD src0_sel:BYTE_0 src1_sel:DWORD
	v_lshlrev_b32_e32 v8, 5, v21
	v_ashrrev_i16_sdwa v2, v235, sext(v2) dst_sel:DWORD dst_unused:UNUSED_PAD src0_sel:DWORD src1_sel:BYTE_0
	s_lshl_b64 s[0:1], s[44:45], 19
	s_lshl_b64 s[4:5], s[4:5], 19
	v_and_b32_e32 v8, 32, v8
	v_bfe_i32 v22, v2, 0, 16
	v_bitop3_b32 v2, v5, s70, v6 bitop3:0xc8
	v_lshrrev_b32_e32 v5, 8, v1
	s_add_u32 s52, s40, s4
	v_add_lshl_u32 v4, v8, v22, 1
	v_add_u32_e32 v2, v2, v5
	s_addc_u32 s53, s41, s5
	s_add_i32 s43, s33, 0
	v_lshl_add_u32 v2, v2, 11, v4
	s_add_i32 m0, s43, 0x10000
	v_lshl_add_u32 v136, v7, 11, v4
	global_load_lds_dwordx4 v2, s[52:53]
	s_add_i32 m0, s43, 0x12000
	v_lshl_add_u32 v138, v1, 11, v4
	global_load_lds_dwordx4 v132, s[52:53]
	s_add_i32 m0, s43, 0x14000
	v_mov_b32_e32 v133, v3
	global_load_lds_dwordx4 v136, s[52:53]
	s_add_i32 m0, s43, 0x16000
	s_add_u32 s46, s38, s0
	s_addc_u32 s47, s39, s1
	s_add_i32 s45, s43, 0x2000
	global_load_lds_dwordx4 v0, s[52:53]
	s_mov_b32 m0, s43
	s_add_u32 s0, s46, 0x40000
	global_load_lds_dwordx4 v138, s[46:47]
	s_mov_b32 m0, s45
	s_addc_u32 s1, s47, 0
	s_add_i32 s48, s43, 0x4000
	global_load_lds_dwordx4 v134, s[46:47]
	s_mov_b32 m0, s48
	s_add_i32 s49, s43, 0x6000
	global_load_lds_dwordx4 v138, s[0:1]
	s_mov_b32 m0, s49
	v_mov_b32_e32 v137, v3
	global_load_lds_dwordx4 v134, s[0:1]
	v_mov_b32_e32 v1, v3
	v_mov_b32_e32 v139, v3
	v_mov_b32_e32 v135, v3
	s_cmp_eq_u32 s7, 1
	v_lshl_add_u64 v[10:11], s[52:53], 0, v[2:3]
	v_lshl_add_u64 v[8:9], s[52:53], 0, v[132:133]
	v_lshl_add_u64 v[6:7], s[52:53], 0, v[136:137]
	v_lshl_add_u64 v[4:5], s[52:53], 0, v[0:1]
	v_lshl_add_u64 v[12:13], s[46:47], 0, v[138:139]
	s_cselect_b64 s[0:1], -1, 0
	s_cmp_lg_u32 s7, 1
	v_lshl_add_u64 v[14:15], s[46:47], 0, v[134:135]
	s_cbranch_scc1 .LBB0_721
	s_barrier
